# layer-1 modulation GEMV inside layer 0's attention phase: 4 weight loads per k-step issued together with counted vmcnt (was load-wait x4), op_sel scalar broadcast; conversion quotas re-balanced (19 /
# speedup vs baseline: 1.0115x; 1.0030x over previous
; __device__ __forceinline__ unsigned xb_ld(unsigned* p)              { return __hip_atomic_load(p, __ATOMIC_RELAXED, __HIP_MEMORY_SCOPE_AGENT); }
; __global__ void __launch_bounds__(512, 2) mk_fwd(Args a) {
;     ...
;     if (hi - lo > 1) {
;         if (c.tid == 0) { unsigned* bw = (unsigned*)(a.ws + WS_CTL) + 4096; bool even = (c.G % 8) == 0;
;             for (unsigned j = 0; j < 8; ++j) even = even && (xb_ld(&bw[XB_XCNT(j)]) == (unsigned)(c.G / 8));
;             MISC[12] = even ? (MISC[10] * 8u + bar.x) : (unsigned)c.bid; }
;         __syncthreads();
;         c.bid = (int)MISC[12];
;     }
.LBB0_174:
	s_andn2_b64 vcc, exec, s[0:1]
	s_cbranch_vccnz .LBB0_188
	v_cmp_eq_u32_e32 vcc, 0, v0
	s_and_saveexec_b64 s[0:1], vcc
	s_cbranch_execz .LBB0_187
	s_and_b32 s4, s91, 7
	s_cmp_lg_u32 s4, 0
	v_mov_b32_e32 v1, s90
	s_cbranch_scc1 .LBB0_186
	s_load_dwordx2 s[4:5], s[36:37], 0xe0
	v_mov_b32_e32 v2, 0x4000
	s_ashr_i32 s6, s91, 31
	s_lshr_b32 s6, s6, 29
	s_add_i32 s6, s91, s6
	s_waitcnt lgkmcnt(0)
	global_load_dword v1, v2, s[4:5] offset:1024 sc1
	global_load_dword v3, v2, s[4:5] offset:1280 sc1
	global_load_dword v4, v2, s[4:5] offset:1536 sc1
	global_load_dword v5, v2, s[4:5] offset:1792 sc1
	global_load_dword v6, v2, s[4:5] offset:2048 sc1
	global_load_dword v7, v2, s[4:5] offset:2304 sc1
	global_load_dword v8, v2, s[4:5] offset:2560 sc1
	global_load_dword v9, v2, s[4:5] offset:2816 sc1
	s_ashr_i32 s6, s6, 3
	s_waitcnt vmcnt(0)
	v_xor_b32_e32 v1, s6, v1
	v_xor_b32_e32 v3, s6, v3
	v_xor_b32_e32 v4, s6, v4
	v_xor_b32_e32 v5, s6, v5
	v_xor_b32_e32 v6, s6, v6
	v_xor_b32_e32 v7, s6, v7
	v_xor_b32_e32 v8, s6, v8
	v_xor_b32_e32 v9, s6, v9
	v_or3_b32 v1, v1, v3, v4
	v_or3_b32 v5, v5, v6, v7
	v_or3_b32 v1, v1, v5, v8
	v_or_b32_e32 v1, v1, v9
	v_cmp_ne_u32_e32 vcc, 0, v1
	v_mov_b32_e32 v1, s90
	s_nop 1
	s_cbranch_vccnz .LBB0_186
	s_add_i32 s4, 0, 0x27028
	v_mov_b32_e32 v1, s4
	ds_read_b32 v1, v1
	s_waitcnt lgkmcnt(0)
	v_lshlrev_b32_e32 v1, 3, v1
	v_add_u32_e32 v1, s33, v1

; __device__ __forceinline__ void mod_items(const Args& a, const Ctx& c0, int l) {
;     ...
;     for (int cb = c.bid; cb < 192; cb += c.G) {
;         const float* w = INP(4) + (size_t)l * DM * NMODW + cb * 64 + cl * 4;
;         f32x4 acc[5];
; #pragma unroll
;         for (int r = 0; r < 5; ++r) acc[r] = (f32x4){0.f, 0.f, 0.f, 0.f};
; #pragma unroll 4
;         for (int k = kg; k < DM; k += 32) { const f32x4 wv = *(const f32x4*)(w + (size_t)k * NMODW);
; #pragma unroll
;             for (int r = 0; r < 5; ++r) acc[r] += sc[r * DM + k] * wv; }
; #pragma unroll
.LBB0_1248:
	v_lshl_add_u64 v[108:109], v[36:37], 0, s[10:11]
	v_lshl_add_u64 v[110:111], v[34:35], 0, s[10:11]
	v_lshl_add_u64 v[112:113], v[32:33], 0, s[10:11]
	v_lshl_add_u64 v[114:115], v[30:31], 0, s[10:11]
	global_load_dwordx4 v[116:119], v[108:109], off
	global_load_dwordx4 v[120:123], v[110:111], off
	global_load_dwordx4 v[124:127], v[112:113], off
	global_load_dwordx4 v[128:131], v[114:115], off
	v_add_u32_e32 v132, 0x2000, v45
	v_add_u32_e32 v133, 0x4000, v45
	v_add_u32_e32 v134, 0x6000, v45
	v_add_u32_e32 v135, 0x8000, v45
	ds_read2_b32 v[46:47], v45 offset1:32
	ds_read2_b32 v[48:49], v45 offset0:64 offset1:96
	ds_read2_b32 v[50:51], v132 offset1:32
	ds_read2_b32 v[52:53], v132 offset0:64 offset1:96
	ds_read2_b32 v[54:55], v133 offset1:32
	ds_read2_b32 v[56:57], v133 offset0:64 offset1:96
	ds_read2_b32 v[58:59], v134 offset1:32
	ds_read2_b32 v[60:61], v134 offset0:64 offset1:96
	ds_read2_b32 v[62:63], v135 offset1:32
	ds_read2_b32 v[136:137], v135 offset0:64 offset1:96
	v_add_u32_e32 v44, 0x80, v44
	v_cmp_lt_i32_e64 s[2:3], s77, v44
	v_lshl_add_u64 v[36:37], v[36:37], 0, s[18:19]
	v_lshl_add_u64 v[34:35], v[34:35], 0, s[18:19]
	v_lshl_add_u64 v[32:33], v[32:33], 0, s[18:19]
	v_lshl_add_u64 v[30:31], v[30:31], 0, s[18:19]
	v_add_u32_e32 v45, 0x200, v45
	s_or_b64 s[16:17], s[2:3], s[16:17]
	s_waitcnt vmcnt(3) lgkmcnt(0)
	v_pk_fma_f32 v[18:19], v[116:117], v[46:47], v[18:19] op_sel_hi:[1,0,1]
	v_pk_fma_f32 v[20:21], v[118:119], v[46:47], v[20:21] op_sel_hi:[1,0,1]
	v_pk_fma_f32 v[14:15], v[116:117], v[50:51], v[14:15] op_sel_hi:[1,0,1]
	v_pk_fma_f32 v[16:17], v[118:119], v[50:51], v[16:17] op_sel_hi:[1,0,1]
	v_pk_fma_f32 v[10:11], v[116:117], v[54:55], v[10:11] op_sel_hi:[1,0,1]
	v_pk_fma_f32 v[12:13], v[118:119], v[54:55], v[12:13] op_sel_hi:[1,0,1]
	v_pk_fma_f32 v[2:3], v[116:117], v[58:59], v[2:3] op_sel_hi:[1,0,1]
	v_pk_fma_f32 v[4:5], v[118:119], v[58:59], v[4:5] op_sel_hi:[1,0,1]
	v_pk_fma_f32 v[6:7], v[116:117], v[62:63], v[6:7] op_sel_hi:[1,0,1]
	v_pk_fma_f32 v[8:9], v[118:119], v[62:63], v[8:9] op_sel_hi:[1,0,1]
	s_waitcnt vmcnt(2)
	v_pk_fma_f32 v[18:19], v[120:121], v[46:47], v[18:19] op_sel:[0,1,0]
	v_pk_fma_f32 v[20:21], v[122:123], v[46:47], v[20:21] op_sel:[0,1,0]
	v_pk_fma_f32 v[14:15], v[120:121], v[50:51], v[14:15] op_sel:[0,1,0]
	v_pk_fma_f32 v[16:17], v[122:123], v[50:51], v[16:17] op_sel:[0,1,0]
	v_pk_fma_f32 v[10:11], v[120:121], v[54:55], v[10:11] op_sel:[0,1,0]
	v_pk_fma_f32 v[12:13], v[122:123], v[54:55], v[12:13] op_sel:[0,1,0]
	v_pk_fma_f32 v[2:3], v[120:121], v[58:59], v[2:3] op_sel:[0,1,0]
	v_pk_fma_f32 v[4:5], v[122:123], v[58:59], v[4:5] op_sel:[0,1,0]
	v_pk_fma_f32 v[6:7], v[120:121], v[62:63], v[6:7] op_sel:[0,1,0]
	v_pk_fma_f32 v[8:9], v[122:123], v[62:63], v[8:9] op_sel:[0,1,0]
	s_waitcnt vmcnt(1)
	v_pk_fma_f32 v[18:19], v[124:125], v[48:49], v[18:19] op_sel_hi:[1,0,1]
	v_pk_fma_f32 v[20:21], v[126:127], v[48:49], v[20:21] op_sel_hi:[1,0,1]
	v_pk_fma_f32 v[14:15], v[124:125], v[52:53], v[14:15] op_sel_hi:[1,0,1]
	v_pk_fma_f32 v[16:17], v[126:127], v[52:53], v[16:17] op_sel_hi:[1,0,1]
	v_pk_fma_f32 v[10:11], v[124:125], v[56:57], v[10:11] op_sel_hi:[1,0,1]
	v_pk_fma_f32 v[12:13], v[126:127], v[56:57], v[12:13] op_sel_hi:[1,0,1]
	v_pk_fma_f32 v[2:3], v[124:125], v[60:61], v[2:3] op_sel_hi:[1,0,1]
	v_pk_fma_f32 v[4:5], v[126:127], v[60:61], v[4:5] op_sel_hi:[1,0,1]
	v_pk_fma_f32 v[6:7], v[124:125], v[136:137], v[6:7] op_sel_hi:[1,0,1]
	v_pk_fma_f32 v[8:9], v[126:127], v[136:137], v[8:9] op_sel_hi:[1,0,1]
	s_waitcnt vmcnt(0)
	v_pk_fma_f32 v[18:19], v[128:129], v[48:49], v[18:19] op_sel:[0,1,0]
	v_pk_fma_f32 v[20:21], v[130:131], v[48:49], v[20:21] op_sel:[0,1,0]
	v_pk_fma_f32 v[14:15], v[128:129], v[52:53], v[14:15] op_sel:[0,1,0]
	v_pk_fma_f32 v[16:17], v[130:131], v[52:53], v[16:17] op_sel:[0,1,0]
	v_pk_fma_f32 v[10:11], v[128:129], v[56:57], v[10:11] op_sel:[0,1,0]
	v_pk_fma_f32 v[12:13], v[130:131], v[56:57], v[12:13] op_sel:[0,1,0]
	v_pk_fma_f32 v[2:3], v[128:129], v[60:61], v[2:3] op_sel:[0,1,0]
	v_pk_fma_f32 v[4:5], v[130:131], v[60:61], v[4:5] op_sel:[0,1,0]
	v_pk_fma_f32 v[6:7], v[128:129], v[136:137], v[6:7] op_sel:[0,1,0]
	v_pk_fma_f32 v[8:9], v[130:131], v[136:137], v[8:9] op_sel:[0,1,0]
	s_andn2_b64 exec, exec, s[16:17]
	s_cbranch_execnz .LBB0_1248
	s_or_b64 exec, exec, s[16:17]

; #define LAS __attribute__((address_space(3)))
; #define PHASE_BEGIN() Ctx c = c0; { int t_ = c0.tid; asm volatile("" : "+v"(t_)); c.tid = t_; c.lane = t_ & 63; c.wave = __builtin_amdgcn_readfirstlane(t_ >> 6); } \
;     GAS unsigned char* wsb = (GAS unsigned char*)a.ws; asm volatile("" : "+s"(wsb));
; __device__ __forceinline__ void bg_take(const Args& a, const Ctx& c0, int n) {
;     PHASE_BEGIN();
;     unsigned* head = WSP(unsigned, WS_CTL) + CW_QHEAD;
;     volatile LAS unsigned* bc = (volatile LAS unsigned*)(c.lds + LDS_MISC + 64);
;     LAS float* scr = (LAS float*)(c.lds + c.wave * 16640);
;     __syncthreads();
;     for (int i = 0; i < n; ++i) {
; __global__ void __launch_bounds__(512, 2) mk_fwd(Args a) {
;     ...
;         if (IN(pb + 5) && (c.bid & 1) == 0) { if (l == 0) mod_items(a, c, 1); bg_take(a, c, l == 0 ? 26 : 24); }
;         if (EN(5) && IN(pb + 5)) for (int rep = 0; rep < NREP(5); ++rep) { phase_attn(a, c, l, last); }
;         if (IN(pb + 5) && (c.bid & 1) == 1) { bg_take(a, c, l == 0 ? 26 : 24); if (l == 0) mod_items(a, c, 1); }
.LBB0_1254:
	s_cmp_lt_u32 s14, 25
	s_cbranch_scc1 .Lbal1_l1
	s_mov_b32 s14, 19
	s_cmp_lt_u32 s90, 32
	s_cbranch_scc0 .Lbal1_b
	s_add_i32 s14, s14, -4
.Lbal1_b:
	s_cmp_gt_u32 s90, 191
	s_cbranch_scc0 .Lbal1_c
	s_add_i32 s14, s14, 7
	s_branch .Lbal1_c

; __global__ void __launch_bounds__(512, 2) mk_fwd(Args a) {
;     ...
;         if (IN(pb + 5) && (c.bid & 1) == 0) { if (l == 0) mod_items(a, c, 1); bg_take(a, c, l == 0 ? 26 : 24); }
;         if (EN(5) && IN(pb + 5)) for (int rep = 0; rep < NREP(5); ++rep) { phase_attn(a, c, l, last); }
;         if (IN(pb + 5) && (c.bid & 1) == 1) { bg_take(a, c, l == 0 ? 26 : 24); if (l == 0) mod_items(a, c, 1); }
.LBB0_1493:
	v_readlane_b32 s2, v252, 54
	v_readlane_b32 s3, v252, 55
	s_andn2_b64 vcc, exec, s[2:3]
	s_cbranch_vccnz .LBB0_1700
	v_readlane_b32 s2, v254, 54
	v_readlane_b32 s3, v254, 55
	s_and_b64 s[2:3], s[2:3], exec
	v_mov_b32_e32 v1, v0
	v_readlane_b32 s4, v254, 21
	v_readlane_b32 s5, v254, 22
	v_readfirstlane_b32 s2, v1
	v_readlane_b32 s6, v254, 23
	v_readlane_b32 s7, v254, 24
	s_cselect_b32 s10, 26, 24
	s_cmp_lt_u32 s10, 25
	s_cbranch_scc1 .Lbal2_l1
	s_mov_b32 s10, 19
	s_cmp_lt_u32 s90, 32
	s_cbranch_scc0 .Lbal2_b
	s_add_i32 s10, s10, -4
.Lbal2_b:
	s_cmp_gt_u32 s90, 191
	s_cbranch_scc0 .Lbal2_c
	s_add_i32 s10, s10, 7
	s_branch .Lbal2_c

; __device__ __forceinline__ void mod_items(const Args& a, const Ctx& c0, int l) {
;     ...
;     for (int cb = c.bid; cb < 192; cb += c.G) {
;         const float* w = INP(4) + (size_t)l * DM * NMODW + cb * 64 + cl * 4;
;         f32x4 acc[5];
; #pragma unroll
;         for (int r = 0; r < 5; ++r) acc[r] = (f32x4){0.f, 0.f, 0.f, 0.f};
; #pragma unroll 4
;         for (int k = kg; k < DM; k += 32) { const f32x4 wv = *(const f32x4*)(w + (size_t)k * NMODW);
; #pragma unroll
;             for (int r = 0; r < 5; ++r) acc[r] += sc[r * DM + k] * wv; }
; #pragma unroll
.LBB0_1695:
	v_lshl_add_u64 v[108:109], v[36:37], 0, s[8:9]
	v_lshl_add_u64 v[110:111], v[34:35], 0, s[8:9]
	v_lshl_add_u64 v[112:113], v[32:33], 0, s[8:9]
	v_lshl_add_u64 v[114:115], v[30:31], 0, s[8:9]
	global_load_dwordx4 v[116:119], v[108:109], off
	global_load_dwordx4 v[120:123], v[110:111], off
	global_load_dwordx4 v[124:127], v[112:113], off
	global_load_dwordx4 v[128:131], v[114:115], off
	v_add_u32_e32 v132, 0x2000, v45
	v_add_u32_e32 v133, 0x4000, v45
	v_add_u32_e32 v134, 0x6000, v45
	v_add_u32_e32 v135, 0x8000, v45
	ds_read2_b32 v[46:47], v45 offset1:32
	ds_read2_b32 v[48:49], v45 offset0:64 offset1:96
	ds_read2_b32 v[50:51], v132 offset1:32
	ds_read2_b32 v[52:53], v132 offset0:64 offset1:96
	ds_read2_b32 v[54:55], v133 offset1:32
	ds_read2_b32 v[56:57], v133 offset0:64 offset1:96
	ds_read2_b32 v[58:59], v134 offset1:32
	ds_read2_b32 v[60:61], v134 offset0:64 offset1:96
	ds_read2_b32 v[62:63], v135 offset1:32
	ds_read2_b32 v[136:137], v135 offset0:64 offset1:96
	v_add_u32_e32 v44, 0x80, v44
	v_cmp_lt_i32_e64 s[2:3], s77, v44
	v_lshl_add_u64 v[36:37], v[36:37], 0, s[16:17]
	v_lshl_add_u64 v[34:35], v[34:35], 0, s[16:17]
	v_lshl_add_u64 v[32:33], v[32:33], 0, s[16:17]
	v_lshl_add_u64 v[30:31], v[30:31], 0, s[16:17]
	v_add_u32_e32 v45, 0x200, v45
	s_or_b64 s[14:15], s[2:3], s[14:15]
	s_waitcnt vmcnt(3) lgkmcnt(0)
	v_pk_fma_f32 v[18:19], v[116:117], v[46:47], v[18:19] op_sel_hi:[1,0,1]
	v_pk_fma_f32 v[20:21], v[118:119], v[46:47], v[20:21] op_sel_hi:[1,0,1]
	v_pk_fma_f32 v[14:15], v[116:117], v[50:51], v[14:15] op_sel_hi:[1,0,1]
	v_pk_fma_f32 v[16:17], v[118:119], v[50:51], v[16:17] op_sel_hi:[1,0,1]
	v_pk_fma_f32 v[10:11], v[116:117], v[54:55], v[10:11] op_sel_hi:[1,0,1]
	v_pk_fma_f32 v[12:13], v[118:119], v[54:55], v[12:13] op_sel_hi:[1,0,1]
	v_pk_fma_f32 v[2:3], v[116:117], v[58:59], v[2:3] op_sel_hi:[1,0,1]
	v_pk_fma_f32 v[4:5], v[118:119], v[58:59], v[4:5] op_sel_hi:[1,0,1]
	v_pk_fma_f32 v[6:7], v[116:117], v[62:63], v[6:7] op_sel_hi:[1,0,1]
	v_pk_fma_f32 v[8:9], v[118:119], v[62:63], v[8:9] op_sel_hi:[1,0,1]
	s_waitcnt vmcnt(2)
	v_pk_fma_f32 v[18:19], v[120:121], v[46:47], v[18:19] op_sel:[0,1,0]
	v_pk_fma_f32 v[20:21], v[122:123], v[46:47], v[20:21] op_sel:[0,1,0]
	v_pk_fma_f32 v[14:15], v[120:121], v[50:51], v[14:15] op_sel:[0,1,0]
	v_pk_fma_f32 v[16:17], v[122:123], v[50:51], v[16:17] op_sel:[0,1,0]
	v_pk_fma_f32 v[10:11], v[120:121], v[54:55], v[10:11] op_sel:[0,1,0]
	v_pk_fma_f32 v[12:13], v[122:123], v[54:55], v[12:13] op_sel:[0,1,0]
	v_pk_fma_f32 v[2:3], v[120:121], v[58:59], v[2:3] op_sel:[0,1,0]
	v_pk_fma_f32 v[4:5], v[122:123], v[58:59], v[4:5] op_sel:[0,1,0]
	v_pk_fma_f32 v[6:7], v[120:121], v[62:63], v[6:7] op_sel:[0,1,0]
	v_pk_fma_f32 v[8:9], v[122:123], v[62:63], v[8:9] op_sel:[0,1,0]
	s_waitcnt vmcnt(1)
	v_pk_fma_f32 v[18:19], v[124:125], v[48:49], v[18:19] op_sel_hi:[1,0,1]
	v_pk_fma_f32 v[20:21], v[126:127], v[48:49], v[20:21] op_sel_hi:[1,0,1]
	v_pk_fma_f32 v[14:15], v[124:125], v[52:53], v[14:15] op_sel_hi:[1,0,1]
	v_pk_fma_f32 v[16:17], v[126:127], v[52:53], v[16:17] op_sel_hi:[1,0,1]
	v_pk_fma_f32 v[10:11], v[124:125], v[56:57], v[10:11] op_sel_hi:[1,0,1]
	v_pk_fma_f32 v[12:13], v[126:127], v[56:57], v[12:13] op_sel_hi:[1,0,1]
	v_pk_fma_f32 v[2:3], v[124:125], v[60:61], v[2:3] op_sel_hi:[1,0,1]
	v_pk_fma_f32 v[4:5], v[126:127], v[60:61], v[4:5] op_sel_hi:[1,0,1]
	v_pk_fma_f32 v[6:7], v[124:125], v[136:137], v[6:7] op_sel_hi:[1,0,1]
	v_pk_fma_f32 v[8:9], v[126:127], v[136:137], v[8:9] op_sel_hi:[1,0,1]
	s_waitcnt vmcnt(0)
	v_pk_fma_f32 v[18:19], v[128:129], v[48:49], v[18:19] op_sel:[0,1,0]
	v_pk_fma_f32 v[20:21], v[130:131], v[48:49], v[20:21] op_sel:[0,1,0]
	v_pk_fma_f32 v[14:15], v[128:129], v[52:53], v[14:15] op_sel:[0,1,0]
	v_pk_fma_f32 v[16:17], v[130:131], v[52:53], v[16:17] op_sel:[0,1,0]
	v_pk_fma_f32 v[10:11], v[128:129], v[56:57], v[10:11] op_sel:[0,1,0]
	v_pk_fma_f32 v[12:13], v[130:131], v[56:57], v[12:13] op_sel:[0,1,0]
	v_pk_fma_f32 v[2:3], v[128:129], v[60:61], v[2:3] op_sel:[0,1,0]
	v_pk_fma_f32 v[4:5], v[130:131], v[60:61], v[4:5] op_sel:[0,1,0]
	v_pk_fma_f32 v[6:7], v[128:129], v[136:137], v[6:7] op_sel:[0,1,0]
	v_pk_fma_f32 v[8:9], v[130:131], v[136:137], v[8:9] op_sel:[0,1,0]
	s_andn2_b64 exec, exec, s[14:15]
	s_cbranch_execnz .LBB0_1695
	s_or_b64 exec, exec, s[14:15]
